# router: slot atomics and list stores of a wave's tokens issued together after the token loop (per-token results parked in LDS)
# baseline (speedup 1.0000x reference)
.LBB0_1619:
	s_or_b64 exec, exec, s[0:1]
	s_lshl_b32 s0, s13, 3
	s_add_i32 s56, s0, s91
	s_cmpk_gt_i32 s56, 0x3fff
	s_waitcnt vmcnt(16) lgkmcnt(0)
	s_barrier
	s_cbranch_scc1 .LBB0_1624
	s_lshl_b32 s58, s12, 3
	s_add_u32 s68, s52, 0x300000
	s_addc_u32 s69, s53, 0
	s_add_u32 s70, s52, 0x380000
	s_addc_u32 s71, s53, 0
	s_add_u32 s2, s52, 0x420000
	s_addc_u32 s3, s53, 0
	s_add_u32 s4, s52, 0x440000
	s_addc_u32 s5, s53, 0
	s_ashr_i32 s57, s56, 31
	s_lshl_b64 s[0:1], s[56:57], 2
	s_add_u32 s8, s0, 0x400000
	v_and_b32_e32 v0, 63, v0
	s_addc_u32 s9, s1, 0
	s_lshl_b64 s[0:1], s[56:57], 12
	s_ashr_i32 s59, s58, 31
	v_lshl_or_b32 v18, v0, 3, s0
	v_mov_b32_e32 v19, s1
	s_lshl_b32 s0, s13, 4
	v_readlane_b32 s1, v254, 53
	v_cmp_eq_u32_e64 s[36:37], 0, v0
	v_lshl_add_u32 v25, v0, 4, 0
	s_lshl_b64 s[72:73], s[58:59], 2
	s_lshl_b64 s[76:77], s[58:59], 12
	s_add_i32 s66, s1, s0
	s_lshl_b32 s12, s12, 4
	s_mov_b32 s98, 0
	s_lshl_b32 s99, s91, 8
	s_add_i32 s99, s99, 0x10000
	s_branch .LBB0_1622

.LBB0_1622:
	v_lshl_add_u64 v[0:1], s[52:53], 0, v[18:19]
	s_waitcnt lgkmcnt(0)
	v_add_co_u32_e32 v20, vcc, 0x2d000000, v0
	s_nop 1
	v_addc_co_u32_e32 v21, vcc, 0, v1, vcc
	global_load_dwordx2 v[60:61], v[20:21], off
	global_load_dwordx2 v[62:63], v[20:21], off offset:512
	global_load_dwordx2 v[64:65], v[20:21], off offset:1024
	global_load_dwordx2 v[66:67], v[20:21], off offset:1536
	global_load_dwordx2 v[68:69], v[20:21], off offset:2048
	global_load_dwordx2 v[70:71], v[20:21], off offset:2560
	global_load_dwordx2 v[72:73], v[20:21], off offset:3072
	global_load_dwordx2 v[74:75], v[20:21], off offset:3584
	s_waitcnt vmcnt(7)
	v_mov_b32_e32 v0, v60
	v_mov_b32_e32 v1, v61
	v_lshlrev_b32_e32 v26, 16, v0
	v_and_b32_e32 v28, 0xffff0000, v0
	v_lshlrev_b32_e32 v30, 16, v1
	v_and_b32_e32 v32, 0xffff0000, v1
	ds_read_b128 v[0:3], v25
	ds_read_b128 v[4:7], v25 offset:32768
	v_mul_f32_e32 v40, v28, v28
	v_fmac_f32_e32 v40, v26, v26
	v_fmac_f32_e32 v40, v30, v30
	s_waitcnt lgkmcnt(1)
	v_fma_f32 v39, v2, v26, 0
	v_fma_f32 v37, v3, v26, 0
	s_waitcnt lgkmcnt(0)
	v_fma_f32 v35, v4, v26, 0
	v_fma_f32 v33, v5, v26, 0
	v_fma_f32 v31, v6, v26, 0
	v_fma_f32 v29, v7, v26, 0
	ds_read_b128 v[2:5], v25 offset:8192
	ds_read_b128 v[6:9], v25 offset:40960
	v_pk_fma_f32 v[0:1], v[0:1], v[26:27], 0 op_sel_hi:[1,0,0]
	v_fmac_f32_e32 v40, v32, v32
	s_waitcnt lgkmcnt(1)
	v_fmac_f32_e32 v39, v4, v28
	v_fmac_f32_e32 v37, v5, v28
	s_waitcnt lgkmcnt(0)
	v_fmac_f32_e32 v35, v6, v28
	v_fmac_f32_e32 v33, v7, v28
	v_fmac_f32_e32 v31, v8, v28
	v_fmac_f32_e32 v29, v9, v28
	ds_read_b128 v[4:7], v25 offset:16384
	ds_read_b128 v[8:11], v25 offset:49152
	s_waitcnt lgkmcnt(1)
	v_fmac_f32_e32 v39, v6, v30
	v_fmac_f32_e32 v37, v7, v30
	s_waitcnt lgkmcnt(0)
	v_fmac_f32_e32 v35, v8, v30
	v_fmac_f32_e32 v33, v9, v30
	v_fmac_f32_e32 v31, v10, v30
	v_fmac_f32_e32 v29, v11, v30
	ds_read_b128 v[6:9], v25 offset:24576
	ds_read_b128 v[10:13], v25 offset:57344
	s_waitcnt lgkmcnt(1)
	v_fmac_f32_e32 v39, v8, v32
	v_fmac_f32_e32 v37, v9, v32
	s_waitcnt lgkmcnt(0)
	v_fmac_f32_e32 v35, v10, v32
	v_fmac_f32_e32 v33, v11, v32
	v_fmac_f32_e32 v31, v12, v32
	v_fmac_f32_e32 v29, v13, v32
	v_pk_fma_f32 v[0:1], v[2:3], v[28:29], v[0:1] op_sel_hi:[1,0,1]
	s_waitcnt vmcnt(6)
	v_mov_b32_e32 v8, v62
	v_mov_b32_e32 v9, v63
	v_lshlrev_b32_e32 v34, 16, v8
	v_and_b32_e32 v16, 0xffff0000, v8
	v_lshlrev_b32_e32 v22, 16, v9
	v_and_b32_e32 v24, 0xffff0000, v9
	ds_read_b128 v[8:11], v25 offset:1024
	ds_read_b128 v[12:15], v25 offset:33792
	v_pk_fma_f32 v[0:1], v[4:5], v[30:31], v[0:1] op_sel_hi:[1,0,1]
	v_fmac_f32_e32 v40, v34, v34
	v_pk_fma_f32 v[0:1], v[6:7], v[32:33], v[0:1] op_sel_hi:[1,0,1]
	s_waitcnt lgkmcnt(1)
	v_fmac_f32_e32 v39, v10, v34
	v_pk_fma_f32 v[26:27], v[8:9], v[34:35], v[0:1] op_sel_hi:[1,0,1]
	ds_read_b128 v[0:3], v25 offset:9216
	ds_read_b128 v[4:7], v25 offset:41984
	v_fmac_f32_e32 v37, v11, v34
	s_waitcnt lgkmcnt(2)
	v_fmac_f32_e32 v35, v12, v34
	v_fmac_f32_e32 v33, v13, v34
	v_fmac_f32_e32 v31, v14, v34
	v_fmac_f32_e32 v29, v15, v34
	s_waitcnt lgkmcnt(1)
	v_fmac_f32_e32 v39, v2, v16
	v_fmac_f32_e32 v37, v3, v16
	s_waitcnt lgkmcnt(0)
	v_fmac_f32_e32 v35, v4, v16
	v_fmac_f32_e32 v33, v5, v16
	v_fmac_f32_e32 v31, v6, v16
	v_fmac_f32_e32 v29, v7, v16
	ds_read_b128 v[2:5], v25 offset:17408
	ds_read_b128 v[6:9], v25 offset:50176
	v_pk_fma_f32 v[0:1], v[0:1], v[16:17], v[26:27] op_sel_hi:[1,0,1]
	v_fmac_f32_e32 v40, v16, v16
	v_fmac_f32_e32 v40, v22, v22
	s_waitcnt lgkmcnt(1)
	v_fmac_f32_e32 v39, v4, v22
	v_fmac_f32_e32 v37, v5, v22
	s_waitcnt lgkmcnt(0)
	v_fmac_f32_e32 v35, v6, v22
	v_fmac_f32_e32 v33, v7, v22
	v_fmac_f32_e32 v31, v8, v22
	v_fmac_f32_e32 v29, v9, v22
	ds_read_b128 v[4:7], v25 offset:25600
	ds_read_b128 v[8:11], v25 offset:58368
	v_pk_fma_f32 v[0:1], v[2:3], v[22:23], v[0:1] op_sel_hi:[1,0,1]
	v_fmac_f32_e32 v40, v24, v24
	s_waitcnt lgkmcnt(1)
	v_fmac_f32_e32 v39, v6, v24
	v_fmac_f32_e32 v37, v7, v24
	s_waitcnt lgkmcnt(0)
	v_fmac_f32_e32 v35, v8, v24
	v_fmac_f32_e32 v33, v9, v24
	v_fmac_f32_e32 v31, v10, v24
	v_fmac_f32_e32 v29, v11, v24
	v_pk_fma_f32 v[0:1], v[4:5], v[24:25], v[0:1] op_sel_hi:[1,0,1]
	s_waitcnt vmcnt(5)
	v_mov_b32_e32 v6, v64
	v_mov_b32_e32 v7, v65
	v_lshlrev_b32_e32 v28, 16, v6
	v_and_b32_e32 v30, 0xffff0000, v6
	v_lshlrev_b32_e32 v32, 16, v7
	v_and_b32_e32 v34, 0xffff0000, v7
	ds_read_b128 v[6:9], v25 offset:2048
	ds_read_b128 v[10:13], v25 offset:34816
	v_fmac_f32_e32 v40, v28, v28
	v_fmac_f32_e32 v40, v30, v30
	v_fmac_f32_e32 v40, v32, v32
	s_waitcnt lgkmcnt(1)
	v_fmac_f32_e32 v39, v8, v28
	v_fmac_f32_e32 v37, v9, v28
	s_waitcnt lgkmcnt(0)
	v_fmac_f32_e32 v35, v10, v28
	v_fmac_f32_e32 v33, v11, v28
	v_fmac_f32_e32 v31, v12, v28
	v_fmac_f32_e32 v29, v13, v28
	ds_read_b128 v[8:11], v25 offset:10240
	ds_read_b128 v[12:15], v25 offset:43008
	v_fmac_f32_e32 v40, v34, v34
	s_waitcnt lgkmcnt(1)
	v_fmac_f32_e32 v39, v10, v30
	v_fmac_f32_e32 v37, v11, v30
	s_waitcnt lgkmcnt(0)
	v_fmac_f32_e32 v35, v12, v30
	v_fmac_f32_e32 v33, v13, v30
	ds_read_b128 v[10:13], v25 offset:18432
	ds_read_b128 v[42:45], v25 offset:51200
	v_fmac_f32_e32 v31, v14, v30
	v_fmac_f32_e32 v29, v15, v30
	s_waitcnt lgkmcnt(1)
	v_fmac_f32_e32 v39, v12, v32
	v_fmac_f32_e32 v37, v13, v32
	s_waitcnt lgkmcnt(0)
	v_fmac_f32_e32 v35, v42, v32
	v_fmac_f32_e32 v33, v43, v32
	v_fmac_f32_e32 v31, v44, v32
	v_fmac_f32_e32 v29, v45, v32
	ds_read_b128 v[12:15], v25 offset:26624
	ds_read_b128 v[42:45], v25 offset:59392
	s_waitcnt lgkmcnt(1)
	v_fmac_f32_e32 v39, v14, v34
	v_fmac_f32_e32 v37, v15, v34
	s_waitcnt lgkmcnt(0)
	v_fmac_f32_e32 v35, v42, v34
	v_fmac_f32_e32 v33, v43, v34
	v_fmac_f32_e32 v31, v44, v34
	v_fmac_f32_e32 v29, v45, v34
	ds_read_b128 v[42:45], v25 offset:3072
	ds_read_b128 v[46:49], v25 offset:35840
	s_waitcnt vmcnt(4)
	v_mov_b32_e32 v14, v66
	v_mov_b32_e32 v15, v67
	v_lshlrev_b32_e32 v36, 16, v14
	s_waitcnt lgkmcnt(1)
	v_fmac_f32_e32 v39, v44, v36
	v_fmac_f32_e32 v37, v45, v36
	s_waitcnt lgkmcnt(0)
	v_fmac_f32_e32 v35, v46, v36
	v_fmac_f32_e32 v33, v47, v36
	v_fmac_f32_e32 v31, v48, v36
	v_fmac_f32_e32 v29, v49, v36
	ds_read_b128 v[44:47], v25 offset:11264
	ds_read_b128 v[48:51], v25 offset:44032
	v_and_b32_e32 v14, 0xffff0000, v14
	v_lshlrev_b32_e32 v38, 16, v15
	v_and_b32_e32 v56, 0xffff0000, v15
	s_waitcnt lgkmcnt(1)
	v_fmac_f32_e32 v39, v46, v14
	v_fmac_f32_e32 v37, v47, v14
	s_waitcnt lgkmcnt(0)
	v_fmac_f32_e32 v35, v48, v14
	v_fmac_f32_e32 v33, v49, v14
	v_fmac_f32_e32 v31, v50, v14
	v_fmac_f32_e32 v29, v51, v14
	ds_read_b128 v[46:49], v25 offset:19456
	ds_read_b128 v[50:53], v25 offset:52224
	v_fmac_f32_e32 v40, v36, v36
	v_fmac_f32_e32 v40, v14, v14
	v_fmac_f32_e32 v40, v38, v38
	s_waitcnt lgkmcnt(1)
	v_fmac_f32_e32 v39, v48, v38
	s_waitcnt lgkmcnt(0)
	v_fmac_f32_e32 v29, v53, v38
	v_fmac_f32_e32 v31, v52, v38
	v_pk_fma_f32 v[0:1], v[6:7], v[28:29], v[0:1] op_sel_hi:[1,0,1]
	v_fmac_f32_e32 v33, v51, v38
	v_pk_fma_f32 v[0:1], v[8:9], v[30:31], v[0:1] op_sel_hi:[1,0,1]
	v_fmac_f32_e32 v35, v50, v38
	v_pk_fma_f32 v[0:1], v[10:11], v[32:33], v[0:1] op_sel_hi:[1,0,1]
	v_fmac_f32_e32 v37, v49, v38
	ds_read_b128 v[48:51], v25 offset:27648
	ds_read_b128 v[52:55], v25 offset:60416
	v_pk_fma_f32 v[0:1], v[12:13], v[34:35], v[0:1] op_sel_hi:[1,0,1]
	v_fmac_f32_e32 v40, v56, v56
	v_pk_fma_f32 v[0:1], v[42:43], v[36:37], v[0:1] op_sel_hi:[1,0,1]
	s_waitcnt lgkmcnt(1)
	v_fmac_f32_e32 v37, v51, v56
	v_pk_fma_f32 v[0:1], v[44:45], v[14:15], v[0:1] op_sel_hi:[1,0,1]
	s_waitcnt lgkmcnt(0)
	v_fmac_f32_e32 v35, v52, v56
	v_pk_fma_f32 v[0:1], v[46:47], v[38:39], v[0:1] op_sel_hi:[1,0,1]
	v_fmac_f32_e32 v39, v50, v56
	v_pk_fma_f32 v[22:23], v[48:49], v[56:57], v[0:1] op_sel_hi:[1,0,1]
	v_fmac_f32_e32 v33, v53, v56
	v_fmac_f32_e32 v31, v54, v56
	v_fmac_f32_e32 v29, v55, v56
	s_waitcnt vmcnt(3)
	v_mov_b32_e32 v0, v68
	v_mov_b32_e32 v1, v69
	v_lshlrev_b32_e32 v24, 16, v0
	v_and_b32_e32 v26, 0xffff0000, v0
	v_lshlrev_b32_e32 v28, 16, v1
	v_and_b32_e32 v30, 0xffff0000, v1
	ds_read_b128 v[0:3], v25 offset:4096
	ds_read_b128 v[4:7], v25 offset:36864
	v_fmac_f32_e32 v40, v24, v24
	v_fmac_f32_e32 v40, v26, v26
	v_fmac_f32_e32 v40, v28, v28
	s_waitcnt lgkmcnt(1)
	v_fmac_f32_e32 v39, v2, v24
	v_fmac_f32_e32 v37, v3, v24
	s_waitcnt lgkmcnt(0)
	v_fmac_f32_e32 v35, v4, v24
	v_fmac_f32_e32 v33, v5, v24
	v_fmac_f32_e32 v31, v6, v24
	v_fmac_f32_e32 v29, v7, v24
	ds_read_b128 v[2:5], v25 offset:12288
	ds_read_b128 v[6:9], v25 offset:45056
	v_pk_fma_f32 v[0:1], v[0:1], v[24:25], v[22:23] op_sel_hi:[1,0,1]
	v_fmac_f32_e32 v40, v30, v30
	s_waitcnt lgkmcnt(1)
	v_fmac_f32_e32 v39, v4, v26
	v_fmac_f32_e32 v37, v5, v26
	s_waitcnt lgkmcnt(0)
	v_fmac_f32_e32 v35, v6, v26
	v_fmac_f32_e32 v33, v7, v26
	v_fmac_f32_e32 v31, v8, v26
	v_fmac_f32_e32 v29, v9, v26
	ds_read_b128 v[4:7], v25 offset:20480
	ds_read_b128 v[8:11], v25 offset:53248
	v_pk_fma_f32 v[0:1], v[2:3], v[26:27], v[0:1] op_sel_hi:[1,0,1]
	s_waitcnt lgkmcnt(1)
	v_fmac_f32_e32 v39, v6, v28
	v_fmac_f32_e32 v37, v7, v28
	s_waitcnt lgkmcnt(0)
	v_fmac_f32_e32 v35, v8, v28
	v_fmac_f32_e32 v33, v9, v28
	v_fmac_f32_e32 v31, v10, v28
	v_fmac_f32_e32 v29, v11, v28
	ds_read_b128 v[6:9], v25 offset:28672
	ds_read_b128 v[10:13], v25 offset:61440
	s_waitcnt lgkmcnt(1)
	v_fmac_f32_e32 v39, v8, v30
	v_fmac_f32_e32 v37, v9, v30
	s_waitcnt lgkmcnt(0)
	v_fmac_f32_e32 v35, v10, v30
	v_fmac_f32_e32 v33, v11, v30
	v_fmac_f32_e32 v31, v12, v30
	v_fmac_f32_e32 v29, v13, v30
	s_waitcnt vmcnt(2)
	v_mov_b32_e32 v8, v70
	v_mov_b32_e32 v9, v71
	v_lshlrev_b32_e32 v32, 16, v8
	v_and_b32_e32 v34, 0xffff0000, v8
	v_lshlrev_b32_e32 v36, 16, v9
	v_and_b32_e32 v38, 0xffff0000, v9
	ds_read_b128 v[8:11], v25 offset:5120
	ds_read_b128 v[12:15], v25 offset:37888
	v_fmac_f32_e32 v40, v32, v32
	v_fmac_f32_e32 v40, v34, v34
	v_fmac_f32_e32 v40, v36, v36
	s_waitcnt lgkmcnt(1)
	v_fmac_f32_e32 v39, v10, v32
	v_fmac_f32_e32 v37, v11, v32
	s_waitcnt lgkmcnt(0)
	v_fmac_f32_e32 v35, v12, v32
	v_fmac_f32_e32 v33, v13, v32
	v_fmac_f32_e32 v31, v14, v32
	v_fmac_f32_e32 v29, v15, v32
	ds_read_b128 v[10:13], v25 offset:13312
	ds_read_b128 v[14:17], v25 offset:46080
	v_fmac_f32_e32 v40, v38, v38
	s_waitcnt lgkmcnt(1)
	v_fmac_f32_e32 v39, v12, v34
	v_fmac_f32_e32 v37, v13, v34
	s_waitcnt lgkmcnt(0)
	v_fmac_f32_e32 v35, v14, v34
	v_fmac_f32_e32 v33, v15, v34
	ds_read_b128 v[12:15], v25 offset:21504
	ds_read_b128 v[42:45], v25 offset:54272
	v_fmac_f32_e32 v31, v16, v34
	v_fmac_f32_e32 v29, v17, v34
	s_waitcnt lgkmcnt(1)
	v_fmac_f32_e32 v39, v14, v36
	v_fmac_f32_e32 v37, v15, v36
	s_waitcnt lgkmcnt(0)
	v_fmac_f32_e32 v35, v42, v36
	v_fmac_f32_e32 v33, v43, v36
	v_fmac_f32_e32 v31, v44, v36
	v_fmac_f32_e32 v29, v45, v36
	ds_read_b128 v[14:17], v25 offset:29696
	ds_read_b128 v[42:45], v25 offset:62464
	s_waitcnt lgkmcnt(1)
	v_fmac_f32_e32 v39, v16, v38
	v_fmac_f32_e32 v37, v17, v38
	s_waitcnt lgkmcnt(0)
	v_fmac_f32_e32 v35, v42, v38
	v_fmac_f32_e32 v33, v43, v38
	v_fmac_f32_e32 v31, v44, v38
	v_fmac_f32_e32 v29, v45, v38
	ds_read_b128 v[42:45], v25 offset:6144
	ds_read_b128 v[46:49], v25 offset:38912
	s_waitcnt vmcnt(1)
	v_mov_b32_e32 v16, v72
	v_mov_b32_e32 v17, v73
	v_lshlrev_b32_e32 v54, 16, v16
	s_waitcnt lgkmcnt(1)
	v_fmac_f32_e32 v39, v44, v54
	v_fmac_f32_e32 v37, v45, v54
	s_waitcnt lgkmcnt(0)
	v_fmac_f32_e32 v35, v46, v54
	v_fmac_f32_e32 v33, v47, v54
	v_fmac_f32_e32 v31, v48, v54
	v_fmac_f32_e32 v29, v49, v54
	ds_read_b128 v[44:47], v25 offset:14336
	ds_read_b128 v[48:51], v25 offset:47104
	v_and_b32_e32 v56, 0xffff0000, v16
	v_lshlrev_b32_e32 v58, 16, v17
	v_and_b32_e32 v16, 0xffff0000, v17
	s_waitcnt lgkmcnt(1)
	v_fmac_f32_e32 v37, v47, v56
	s_waitcnt lgkmcnt(0)
	v_fmac_f32_e32 v29, v51, v56
	v_fmac_f32_e32 v31, v50, v56
	v_pk_fma_f32 v[0:1], v[4:5], v[28:29], v[0:1] op_sel_hi:[1,0,1]
	v_fmac_f32_e32 v33, v49, v56
	v_pk_fma_f32 v[0:1], v[6:7], v[30:31], v[0:1] op_sel_hi:[1,0,1]
	v_fmac_f32_e32 v35, v48, v56
	v_pk_fma_f32 v[0:1], v[8:9], v[32:33], v[0:1] op_sel_hi:[1,0,1]
	v_fmac_f32_e32 v39, v46, v56
	v_pk_fma_f32 v[0:1], v[10:11], v[34:35], v[0:1] op_sel_hi:[1,0,1]
	ds_read_b128 v[46:49], v25 offset:22528
	ds_read_b128 v[50:53], v25 offset:55296
	v_pk_fma_f32 v[0:1], v[12:13], v[36:37], v[0:1] op_sel_hi:[1,0,1]
	v_fmac_f32_e32 v40, v54, v54
	v_pk_fma_f32 v[0:1], v[14:15], v[38:39], v[0:1] op_sel_hi:[1,0,1]
	s_waitcnt lgkmcnt(1)
	v_fmac_f32_e32 v39, v48, v58
	v_pk_fma_f32 v[0:1], v[42:43], v[54:55], v[0:1] op_sel_hi:[1,0,1]
	v_fmac_f32_e32 v37, v49, v58
	v_pk_fma_f32 v[0:1], v[44:45], v[56:57], v[0:1] op_sel_hi:[1,0,1]
	s_waitcnt lgkmcnt(0)
	v_fmac_f32_e32 v35, v50, v58
	v_pk_fma_f32 v[12:13], v[46:47], v[58:59], v[0:1] op_sel_hi:[1,0,1]
	ds_read_b128 v[0:3], v25 offset:30720
	ds_read_b128 v[4:7], v25 offset:63488
	v_fmac_f32_e32 v33, v51, v58
	v_fmac_f32_e32 v31, v52, v58
	v_fmac_f32_e32 v29, v53, v58
	s_waitcnt lgkmcnt(1)
	v_fmac_f32_e32 v39, v2, v16
	v_fmac_f32_e32 v37, v3, v16
	s_waitcnt lgkmcnt(0)
	v_fmac_f32_e32 v35, v4, v16
	v_fmac_f32_e32 v33, v5, v16
	v_fmac_f32_e32 v31, v6, v16
	v_fmac_f32_e32 v29, v7, v16
	v_fmac_f32_e32 v40, v56, v56
	v_fmac_f32_e32 v40, v58, v58
	v_fmac_f32_e32 v40, v16, v16
	s_waitcnt vmcnt(0)
	v_mov_b32_e32 v2, v74
	v_mov_b32_e32 v3, v75
	v_lshlrev_b32_e32 v24, 16, v2
	v_and_b32_e32 v22, 0xffff0000, v2
	v_lshlrev_b32_e32 v20, 16, v3
	v_and_b32_e32 v14, 0xffff0000, v3
	ds_read_b128 v[2:5], v25 offset:7168
	ds_read_b128 v[6:9], v25 offset:39936
	v_fmac_f32_e32 v40, v24, v24
	v_fmac_f32_e32 v40, v22, v22
	v_fmac_f32_e32 v40, v20, v20
	s_waitcnt lgkmcnt(1)
	v_fmac_f32_e32 v39, v4, v24
	v_fmac_f32_e32 v37, v5, v24
	s_waitcnt lgkmcnt(0)
	v_fmac_f32_e32 v35, v6, v24
	v_fmac_f32_e32 v33, v7, v24
	v_fmac_f32_e32 v31, v8, v24
	v_fmac_f32_e32 v29, v9, v24
	ds_read_b128 v[4:7], v25 offset:15360
	ds_read_b128 v[8:11], v25 offset:48128
	v_fmac_f32_e32 v40, v14, v14
	s_waitcnt lgkmcnt(1)
	v_fmac_f32_e32 v39, v6, v22
	v_fmac_f32_e32 v37, v7, v22
	s_waitcnt lgkmcnt(0)
	v_fmac_f32_e32 v35, v8, v22
	v_fmac_f32_e32 v33, v9, v22
	ds_read_b128 v[6:9], v25 offset:23552
	ds_read_b128 v[42:45], v25 offset:56320
	v_fmac_f32_e32 v31, v10, v22
	v_fmac_f32_e32 v29, v11, v22
	s_waitcnt lgkmcnt(1)
	v_fmac_f32_e32 v39, v8, v20
	v_fmac_f32_e32 v37, v9, v20
	s_waitcnt lgkmcnt(0)
	v_fmac_f32_e32 v35, v42, v20
	v_fmac_f32_e32 v33, v43, v20
	v_fmac_f32_e32 v31, v44, v20
	v_fmac_f32_e32 v29, v45, v20
	ds_read_b128 v[8:11], v25 offset:31744
	ds_read_b128 v[42:45], v25 offset:64512
	s_waitcnt lgkmcnt(1)
	v_fmac_f32_e32 v39, v10, v14
	v_mbcnt_lo_u32_b32 v10, -1, 0
	v_mbcnt_hi_u32_b32 v10, -1, v10
	v_fmac_f32_e32 v37, v11, v14
	v_lshlrev_b32_e32 v10, 2, v10
	v_xor_b32_e32 v10, 4, v10
	ds_bpermute_b32 v10, v10, v40
	v_mbcnt_lo_u32_b32 v11, -1, 0
	v_mbcnt_hi_u32_b32 v11, -1, v11
	s_waitcnt lgkmcnt(1)
	v_fmac_f32_e32 v35, v42, v14
	v_lshlrev_b32_e32 v11, 2, v11
	v_xor_b32_e32 v11, 8, v11
	s_waitcnt lgkmcnt(0)
	v_add_f32_e32 v10, v40, v10
	ds_bpermute_b32 v11, v11, v10
	v_fmac_f32_e32 v33, v43, v14
	v_fmac_f32_e32 v31, v44, v14
	v_fmac_f32_e32 v29, v45, v14
	s_waitcnt lgkmcnt(0)
	v_add_f32_e32 v10, v10, v11
	v_mbcnt_lo_u32_b32 v11, -1, 0
	v_mbcnt_hi_u32_b32 v11, -1, v11
	s_nop 0
	v_lshlrev_b32_e32 v11, 2, v11
	v_xor_b32_e32 v11, 16, v11
	ds_bpermute_b32 v11, v11, v10
	s_waitcnt lgkmcnt(0)
	v_add_f32_e32 v10, v10, v11
	v_mbcnt_lo_u32_b32 v11, -1, 0
	v_mbcnt_hi_u32_b32 v11, -1, v11
	s_nop 0
	v_lshlrev_b32_e32 v11, 2, v11
	v_xor_b32_e32 v11, 32, v11
	ds_bpermute_b32 v11, v11, v10
	s_waitcnt lgkmcnt(0)
	v_add_f32_e32 v10, v10, v11
	v_mbcnt_lo_u32_b32 v11, -1, 0
	v_mbcnt_hi_u32_b32 v11, -1, v11
	s_nop 0
	v_lshlrev_b32_e32 v11, 2, v11
	v_xor_b32_e32 v11, 64, v11
	ds_bpermute_b32 v11, v11, v10
	s_waitcnt lgkmcnt(0)
	v_add_f32_e32 v10, v10, v11
	v_mbcnt_lo_u32_b32 v11, -1, 0
	v_mbcnt_hi_u32_b32 v11, -1, v11
	v_mbcnt_lo_u32_b32 v15, -1, 0
	v_mbcnt_hi_u32_b32 v15, -1, v15
	v_mbcnt_lo_u32_b32 v17, -1, 0
	v_mbcnt_hi_u32_b32 v17, -1, v17
	v_mbcnt_lo_u32_b32 v21, -1, 0
	v_mbcnt_hi_u32_b32 v21, -1, v21
	v_mbcnt_lo_u32_b32 v23, -1, 0
	v_mbcnt_hi_u32_b32 v23, -1, v23
	v_mbcnt_lo_u32_b32 v26, -1, 0
	v_mbcnt_hi_u32_b32 v26, -1, v26
	v_mbcnt_lo_u32_b32 v27, -1, 0
	v_mbcnt_hi_u32_b32 v27, -1, v27
	s_nop 0
	v_lshlrev_b32_e32 v15, 2, v15
	v_lshlrev_b32_e32 v17, 2, v17
	v_xor_b32_e32 v17, 8, v17
	v_lshlrev_b32_e32 v23, 2, v23
	v_pk_fma_f32 v[0:1], v[0:1], v[16:17], v[12:13] op_sel_hi:[1,0,1]
	v_lshlrev_b32_e32 v21, 2, v21
	v_xor_b32_e32 v23, 32, v23
	v_pk_fma_f32 v[0:1], v[2:3], v[24:25], v[0:1] op_sel_hi:[1,0,1]
	v_xor_b32_e32 v21, 16, v21
	v_mbcnt_lo_u32_b32 v28, -1, 0
	v_mbcnt_hi_u32_b32 v28, -1, v28
	v_pk_fma_f32 v[0:1], v[4:5], v[22:23], v[0:1] op_sel_hi:[1,0,1]
	v_xor_b32_e32 v15, 4, v15
	v_lshlrev_b32_e32 v28, 2, v28
	v_pk_fma_f32 v[0:1], v[6:7], v[20:21], v[0:1] op_sel_hi:[1,0,1]
	v_xor_b32_e32 v28, 4, v28
	v_pk_fma_f32 v[0:1], v[8:9], v[14:15], v[0:1] op_sel_hi:[1,0,1]
	v_mbcnt_lo_u32_b32 v41, -1, 0
	v_mbcnt_hi_u32_b32 v41, -1, v41
	v_lshlrev_b32_e32 v41, 2, v41
	v_xor_b32_e32 v42, 4, v41
	ds_bpermute_b32 v2, v42, v0
	ds_bpermute_b32 v3, v42, v1
	ds_bpermute_b32 v43, v42, v39
	ds_bpermute_b32 v44, v42, v37
	ds_bpermute_b32 v45, v42, v35
	ds_bpermute_b32 v46, v42, v33
	ds_bpermute_b32 v47, v42, v31
	ds_bpermute_b32 v48, v42, v29
	s_waitcnt lgkmcnt(0)
	v_pk_add_f32 v[0:1], v[0:1], v[2:3]
	v_add_f32_e32 v39, v39, v43
	v_add_f32_e32 v37, v37, v44
	v_add_f32_e32 v35, v35, v45
	v_add_f32_e32 v33, v33, v46
	v_add_f32_e32 v31, v31, v47
	v_add_f32_e32 v29, v29, v48
	v_xor_b32_e32 v42, 8, v41
	ds_bpermute_b32 v2, v42, v0
	ds_bpermute_b32 v3, v42, v1
	ds_bpermute_b32 v43, v42, v39
	ds_bpermute_b32 v44, v42, v37
	ds_bpermute_b32 v45, v42, v35
	ds_bpermute_b32 v46, v42, v33
	ds_bpermute_b32 v47, v42, v31
	ds_bpermute_b32 v48, v42, v29
	s_waitcnt lgkmcnt(0)
	v_pk_add_f32 v[0:1], v[0:1], v[2:3]
	v_add_f32_e32 v39, v39, v43
	v_add_f32_e32 v37, v37, v44
	v_add_f32_e32 v35, v35, v45
	v_add_f32_e32 v33, v33, v46
	v_add_f32_e32 v31, v31, v47
	v_add_f32_e32 v29, v29, v48
	v_xor_b32_e32 v42, 16, v41
	ds_bpermute_b32 v2, v42, v0
	ds_bpermute_b32 v3, v42, v1
	ds_bpermute_b32 v43, v42, v39
	ds_bpermute_b32 v44, v42, v37
	ds_bpermute_b32 v45, v42, v35
	ds_bpermute_b32 v46, v42, v33
	ds_bpermute_b32 v47, v42, v31
	ds_bpermute_b32 v48, v42, v29
	s_waitcnt lgkmcnt(0)
	v_pk_add_f32 v[0:1], v[0:1], v[2:3]
	v_add_f32_e32 v39, v39, v43
	v_add_f32_e32 v37, v37, v44
	v_add_f32_e32 v35, v35, v45
	v_add_f32_e32 v33, v33, v46
	v_add_f32_e32 v31, v31, v47
	v_add_f32_e32 v29, v29, v48
	v_xor_b32_e32 v42, 32, v41
	ds_bpermute_b32 v2, v42, v0
	ds_bpermute_b32 v3, v42, v1
	ds_bpermute_b32 v43, v42, v39
	ds_bpermute_b32 v44, v42, v37
	ds_bpermute_b32 v45, v42, v35
	ds_bpermute_b32 v46, v42, v33
	ds_bpermute_b32 v47, v42, v31
	ds_bpermute_b32 v48, v42, v29
	s_waitcnt lgkmcnt(0)
	v_pk_add_f32 v[0:1], v[0:1], v[2:3]
	v_add_f32_e32 v39, v39, v43
	v_add_f32_e32 v37, v37, v44
	v_add_f32_e32 v35, v35, v45
	v_add_f32_e32 v33, v33, v46
	v_add_f32_e32 v31, v31, v47
	v_add_f32_e32 v29, v29, v48
	v_xor_b32_e32 v42, 64, v41
	ds_bpermute_b32 v2, v42, v0
	ds_bpermute_b32 v3, v42, v1
	ds_bpermute_b32 v43, v42, v39
	ds_bpermute_b32 v44, v42, v37
	ds_bpermute_b32 v45, v42, v35
	ds_bpermute_b32 v46, v42, v33
	ds_bpermute_b32 v47, v42, v31
	ds_bpermute_b32 v48, v42, v29
	s_waitcnt lgkmcnt(0)
	v_pk_add_f32 v[0:1], v[0:1], v[2:3]
	v_add_f32_e32 v39, v39, v43
	v_add_f32_e32 v37, v37, v44
	v_add_f32_e32 v35, v35, v45
	v_add_f32_e32 v33, v33, v46
	v_add_f32_e32 v31, v31, v47
	v_add_f32_e32 v29, v29, v48
	v_xor_b32_e32 v42, 0x80, v41
	ds_bpermute_b32 v2, v42, v0
	ds_bpermute_b32 v3, v42, v1
	ds_bpermute_b32 v11, v42, v10
	ds_bpermute_b32 v6, v42, v39
	ds_bpermute_b32 v8, v42, v37
	ds_bpermute_b32 v12, v42, v35
	ds_bpermute_b32 v14, v42, v33
	ds_bpermute_b32 v16, v42, v31
	ds_bpermute_b32 v20, v42, v29
	v_mov_b32_e32 v5, v39
	v_mov_b32_e32 v7, v37
	v_mov_b32_e32 v9, v35
	v_mov_b32_e32 v13, v33
	v_mov_b32_e32 v15, v31
	v_mov_b32_e32 v17, v29
	s_waitcnt lgkmcnt(0)
	s_and_saveexec_b64 s[0:1], s[36:37]
	s_cbranch_execz .LBB0_1621
	v_add_f32_e32 v4, v10, v11
	v_fmamk_f32 v4, v4, 0x3a000000, v253
	s_mov_b32 s13, 0xf800000
	v_cmp_gt_f32_e32 vcc, s13, v4
	v_mul_f32_e32 v10, 0x4f800000, v4
	v_add_f32_e32 v5, v5, v6
	v_cndmask_b32_e32 v4, v4, v10, vcc
	v_sqrt_f32_e32 v10, v4
	v_pk_add_f32 v[0:1], v[0:1], v[2:3]
	v_add_f32_e32 v7, v7, v8
	v_add_f32_e32 v9, v9, v12
	v_add_u32_e32 v11, -1, v10
	v_fma_f32 v21, -v11, v10, v4
	v_cmp_ge_f32_e64 s[38:39], 0, v21
	v_add_u32_e32 v21, 1, v10
	v_add_f32_e32 v13, v13, v14
	v_cndmask_b32_e64 v11, v10, v11, s[38:39]
	v_fma_f32 v10, -v21, v10, v4
	v_cmp_lt_f32_e64 s[38:39], 0, v10
	s_nop 1
	v_cndmask_b32_e64 v10, v11, v21, s[38:39]
	v_mul_f32_e32 v11, 0x37800000, v10
	v_cndmask_b32_e32 v10, v10, v11, vcc
	v_mov_b32_e32 v11, 0x260
	v_cmp_class_f32_e32 vcc, v4, v11
	s_nop 1
	v_cndmask_b32_e32 v4, v10, v4, vcc
	v_div_scale_f32 v10, s[18:19], v4, v4, 1.0
	v_rcp_f32_e32 v11, v10
	s_nop 0
	v_fma_f32 v21, -v10, v11, 1.0
	v_fmac_f32_e32 v11, v21, v11
	v_div_scale_f32 v21, vcc, 1.0, v4, 1.0
	v_mul_f32_e32 v22, v21, v11
	v_fma_f32 v23, -v10, v22, v21
	v_fmac_f32_e32 v22, v23, v11
	v_fma_f32 v10, -v10, v22, v21
	v_div_fmas_f32 v10, v10, v11, v22
	v_div_fixup_f32 v4, v10, v4, 1.0
	v_mul_f32_e32 v5, v4, v5
	v_pk_mul_f32 v[0:1], v[4:5], v[0:1] op_sel_hi:[0,1]
	v_cmp_gt_f32_e32 vcc, v1, v0
	v_mul_f32_e32 v7, v4, v7
	v_mul_f32_e32 v9, v4, v9
	v_cndmask_b32_e32 v2, v0, v1, vcc
	v_cmp_gt_f32_e64 s[38:39], v5, v2
	v_mul_f32_e32 v13, v4, v13
	v_cndmask_b32_e64 v3, 0, 1, vcc
	v_cndmask_b32_e64 v2, v2, v5, s[38:39]
	v_cmp_gt_f32_e64 s[40:41], v7, v2
	v_add_f32_e32 v11, v15, v16
	v_cndmask_b32_e64 v3, v3, 2, s[38:39]
	v_cndmask_b32_e64 v2, v2, v7, s[40:41]
	v_cmp_gt_f32_e64 s[42:43], v9, v2
	v_mul_f32_e32 v11, v4, v11
	v_cndmask_b32_e64 v3, v3, 3, s[40:41]
	v_cndmask_b32_e64 v2, v2, v9, s[42:43]
	v_cmp_gt_f32_e64 s[44:45], v13, v2
	s_waitcnt lgkmcnt(0)
	v_add_f32_e32 v10, v17, v20
	v_cndmask_b32_e64 v3, v3, 4, s[42:43]
	v_cndmask_b32_e64 v2, v2, v13, s[44:45]
	v_cmp_gt_f32_e64 s[46:47], v11, v2
	v_mul_f32_e32 v10, v4, v10
	v_cndmask_b32_e64 v3, v3, 5, s[44:45]
	v_cndmask_b32_e64 v2, v2, v11, s[46:47]
	v_cmp_ngt_f32_e64 s[48:49], v10, v2
	v_cndmask_b32_e64 v3, v3, 6, s[46:47]
	s_and_b64 s[18:19], s[48:49], s[46:47]
	v_cndmask_b32_e64 v176, 7, v3, s[48:49]
	v_cmp_ne_u32_e64 s[46:47], 0, v176
	v_cmp_lt_f32_e64 s[50:51], s11, v0
	s_and_b64 s[46:47], s[46:47], s[50:51]
	v_mov_b32_e32 v3, 0xff61b1e6
	v_cndmask_b32_e64 v0, v3, v0, s[46:47]
	v_cmp_ne_u32_e64 s[44:45], 1, v176
	v_cmp_gt_f32_e64 s[46:47], v1, v0
	s_and_b64 s[44:45], s[44:45], s[46:47]
	v_cndmask_b32_e64 v0, v0, v1, s[44:45]
	v_cmp_ne_u32_e64 s[42:43], 2, v176
	v_cmp_gt_f32_e64 s[46:47], v5, v0
	s_and_b64 s[42:43], s[42:43], s[46:47]
	v_cndmask_b32_e64 v0, v0, v5, s[42:43]
	v_cmp_ne_u32_e64 s[40:41], 3, v176
	v_cmp_gt_f32_e64 s[46:47], v7, v0
	s_and_b64 s[40:41], s[40:41], s[46:47]
	v_cndmask_b32_e64 v0, v0, v7, s[40:41]
	v_cmp_ne_u32_e64 s[38:39], 4, v176
	v_cmp_gt_f32_e64 s[46:47], v9, v0
	s_and_b64 s[38:39], s[38:39], s[46:47]
	v_cndmask_b32_e64 v0, v0, v9, s[38:39]
	v_cmp_ne_u32_e32 vcc, 5, v176
	v_cmp_gt_f32_e64 s[46:47], v13, v0
	s_and_b64 vcc, vcc, s[46:47]
	v_cndmask_b32_e32 v0, v0, v13, vcc
	v_cmp_ngt_f32_e64 s[46:47], v11, v0
	s_or_b64 s[46:47], s[18:19], s[46:47]
	v_cndmask_b32_e64 v2, v10, v2, s[48:49]
	v_cndmask_b32_e64 v1, v11, v0, s[46:47]
	v_cmp_gt_f32_e64 s[50:51], v10, v1
	s_and_b64 s[50:51], s[48:49], s[50:51]
	v_cndmask_b32_e64 v0, 0, 1, s[44:45]
	v_cndmask_b32_e64 v1, v1, v10, s[50:51]
	v_sub_f32_e32 v1, v2, v1
	v_mul_f32_e32 v1, 0x3fb8aa3b, v1
	v_exp_f32_e32 v1, v1
	v_cndmask_b32_e64 v0, v0, 2, s[42:43]
	v_cndmask_b32_e64 v0, v0, 3, s[40:41]
	v_cndmask_b32_e64 v0, v0, 4, s[38:39]
	v_add_f32_e32 v1, 1.0, v1
	v_div_scale_f32 v2, s[18:19], v1, v1, 1.0
	v_rcp_f32_e32 v3, v2
	v_cndmask_b32_e64 v0, v0, 5, vcc
	s_add_u32 s18, s52, s8
	s_addc_u32 s19, s53, s9
	v_fma_f32 v5, -v2, v3, 1.0
	v_fmac_f32_e32 v3, v5, v3
	v_div_scale_f32 v5, vcc, 1.0, v1, 1.0
	v_mul_f32_e32 v6, v5, v3
	v_fma_f32 v7, -v2, v6, v5
	v_fmac_f32_e32 v6, v7, v3
	v_fma_f32 v2, -v2, v6, v5
	v_div_fmas_f32 v2, v2, v3, v6
	v_div_fixup_f32 v5, v2, v1, 1.0
	v_cndmask_b32_e64 v0, 6, v0, s[46:47]
	v_cndmask_b32_e64 v0, v0, 7, s[50:51]
	v_sub_f32_e32 v10, 1.0, v5
	v_mov_b32_e32 v80, v176
	v_mov_b32_e32 v81, v0
	v_mov_b32_e32 v82, v4
	v_mov_b32_e32 v83, v10
	v_mov_b32_e32 v84, v5
	v_mov_b32_e32 v85, s56
	v_mov_b32_e32 v6, s99
	ds_write_b128 v6, v[80:83]
	ds_write_b64 v6, v[84:85] offset:16
	s_add_i32 s99, s99, 32
	s_add_i32 s98, s98, 1
	s_branch .LBB0_1621
.Lrt_flush:
	s_lshl_b32 s18, 1, s98
	s_add_i32 s18, s18, -1
	s_mov_b32 s19, 0
	s_mov_b64 exec, s[18:19]
	v_mbcnt_lo_u32_b32 v6, -1, 0
	v_mbcnt_hi_u32_b32 v6, -1, v6
	s_lshl_b32 s20, s91, 8
	s_add_i32 s20, s20, 0x10000
	v_lshl_add_u32 v6, v6, 5, s20
	s_waitcnt lgkmcnt(0)
	ds_read_b128 v[80:83], v6
	ds_read_b64 v[84:85], v6 offset:16
	s_add_u32 s20, s52, 0x400000
	s_addc_u32 s21, s53, 0
	s_waitcnt lgkmcnt(0)
	v_mul_u32_u24_e32 v86, 0x2100, v80
	v_mul_u32_u24_e32 v87, 0x2100, v81
	global_atomic_add v88, v86, v231, s[52:53] offset:384 sc0
	global_atomic_add v89, v87, v231, s[52:53] offset:384 sc0
	v_lshlrev_b32_e32 v90, 2, v85
	global_store_dword v90, v82, s[20:21]
	v_lshlrev_b32_e32 v91, 3, v85
	v_mov_b32_e32 v92, v83
	v_mov_b32_e32 v93, v84
	global_store_dwordx2 v91, v[92:93], s[4:5]
	s_waitcnt vmcnt(3)
	v_lshl_add_u32 v94, v80, 14, v88
	s_waitcnt vmcnt(2)
	v_lshl_add_u32 v95, v81, 14, v89
	v_lshlrev_b32_e32 v96, 2, v94
	v_lshlrev_b32_e32 v97, 2, v95
	global_store_dword v96, v85, s[68:69]
	global_store_dword v97, v85, s[68:69]
	global_store_dword v96, v82, s[70:71]
	global_store_dword v97, v82, s[70:71]
	global_store_dwordx2 v91, v[94:95], s[2:3]
	s_mov_b64 exec, -1
